# attention step loops (7.12 full): vm_wait ladder replaced by fast tests for the common budgets (6, >=22, 12) + short ladder + one wait-and-branch stub per level
# baseline (speedup 1.0000x reference)
.LBB0_679:
	v_add_co_u32_e64 v66, s[80:81], s87, 1
	s_nop 0
	v_readfirstlane_b32 s68, v66
	s_min_u32 s68, s68, 3
	s_lshl_b32 s68, s68, 1
	s_cmp_gt_i32 s73, 63
	s_cselect_b64 s[84:85], -1, 0
	s_and_b64 vcc, s[84:85], exec
	s_cselect_b32 s79, 8, 16
	s_min_i32 vcc_lo, s87, 2
	s_lshl_b32 vcc_lo, vcc_lo, 1
	s_add_i32 vcc_lo, vcc_lo, 8
	s_and_b64 s[80:81], s[80:81], exec
	s_cselect_b32 s80, 8, vcc_lo
	s_and_b32 s81, s78, -2
	s_or_b32 s79, s68, s79
	s_cmp_eq_u32 s78, 4
	s_cselect_b32 s68, s80, s68
	s_cmp_eq_u32 s81, 2
	s_cselect_b32 s68, s79, s68
	s_cmp_eq_u32 s68, 6
	s_cbranch_scc1 mkvw0_6
	s_cmp_gt_u32 s68, 21
	s_cbranch_scc1 mkvw0_22
	s_cmp_eq_u32 s68, 12
	s_cbranch_scc1 mkvw0_12
	s_cmp_gt_u32 s68, 19
	s_cbranch_scc1 mkvw0_20
	s_cmp_gt_u32 s68, 17
	s_cbranch_scc1 mkvw0_18
	s_cmp_gt_u32 s68, 15
	s_cbranch_scc1 mkvw0_16
	s_cmp_gt_u32 s68, 13
	s_cbranch_scc1 mkvw0_14
	s_cmp_gt_u32 s68, 11
	s_cbranch_scc1 mkvw0_12
	s_cmp_gt_u32 s68, 9
	s_cbranch_scc1 mkvw0_10
	s_cmp_gt_u32 s68, 7
	s_cbranch_scc1 mkvw0_8
	s_cmp_gt_u32 s68, 5
	s_cbranch_scc1 mkvw0_6
	s_cmp_gt_u32 s68, 3
	s_cbranch_scc1 mkvw0_4
	s_cmp_gt_u32 s68, 1
	s_cbranch_scc1 mkvw0_2
mkvw0_0:
	s_waitcnt vmcnt(0)
	s_branch .LBB0_723
mkvw0_2:
	s_waitcnt vmcnt(2)
	s_branch .LBB0_723
mkvw0_4:
	s_waitcnt vmcnt(4)
	s_branch .LBB0_723
mkvw0_8:
	s_waitcnt vmcnt(8)
	s_branch .LBB0_723
mkvw0_10:
	s_waitcnt vmcnt(10)
	s_branch .LBB0_723
mkvw0_14:
	s_waitcnt vmcnt(14)
	s_branch .LBB0_723
mkvw0_16:
	s_waitcnt vmcnt(16)
	s_branch .LBB0_723
mkvw0_18:
	s_waitcnt vmcnt(18)
	s_branch .LBB0_723
mkvw0_20:
	s_waitcnt vmcnt(20)
	s_branch .LBB0_723
mkvw0_12:
	s_waitcnt vmcnt(12)
	s_branch .LBB0_723
mkvw0_22:
	s_waitcnt vmcnt(22)
	s_branch .LBB0_723
mkvw0_6:
	s_waitcnt vmcnt(6)

.LBB0_749:
	v_add_co_u32_e64 v66, s[80:81], s72, 1
	s_nop 0
	v_readfirstlane_b32 s68, v66
	s_min_u32 s68, s68, 3
	s_lshl_b32 s68, s68, 1
	s_cmp_gt_i32 s73, 63
	s_cselect_b64 s[84:85], -1, 0
	s_and_b64 vcc, s[84:85], exec
	s_cselect_b32 s79, 8, 16
	s_min_i32 vcc_lo, s72, 2
	s_lshl_b32 vcc_lo, vcc_lo, 1
	s_add_i32 vcc_lo, vcc_lo, 8
	s_and_b64 s[80:81], s[80:81], exec
	s_cselect_b32 s80, 8, vcc_lo
	s_and_b32 s81, s78, -2
	s_or_b32 s79, s68, s79
	s_cmp_eq_u32 s78, 4
	s_cselect_b32 s68, s80, s68
	s_cmp_eq_u32 s81, 2
	s_cselect_b32 s68, s79, s68
	s_cmp_eq_u32 s68, 6
	s_cbranch_scc1 mkvw1_6
	s_cmp_gt_u32 s68, 21
	s_cbranch_scc1 mkvw1_22
	s_cmp_eq_u32 s68, 12
	s_cbranch_scc1 mkvw1_12
	s_cmp_gt_u32 s68, 19
	s_cbranch_scc1 mkvw1_20
	s_cmp_gt_u32 s68, 17
	s_cbranch_scc1 mkvw1_18
	s_cmp_gt_u32 s68, 15
	s_cbranch_scc1 mkvw1_16
	s_cmp_gt_u32 s68, 13
	s_cbranch_scc1 mkvw1_14
	s_cmp_gt_u32 s68, 11
	s_cbranch_scc1 mkvw1_12
	s_cmp_gt_u32 s68, 9
	s_cbranch_scc1 mkvw1_10
	s_cmp_gt_u32 s68, 7
	s_cbranch_scc1 mkvw1_8
	s_cmp_gt_u32 s68, 5
	s_cbranch_scc1 mkvw1_6
	s_cmp_gt_u32 s68, 3
	s_cbranch_scc1 mkvw1_4
	s_cmp_gt_u32 s68, 1
	s_cbranch_scc1 mkvw1_2
mkvw1_0:
	s_waitcnt vmcnt(0)
	s_branch .LBB0_793
mkvw1_2:
	s_waitcnt vmcnt(2)
	s_branch .LBB0_793
mkvw1_4:
	s_waitcnt vmcnt(4)
	s_branch .LBB0_793
mkvw1_8:
	s_waitcnt vmcnt(8)
	s_branch .LBB0_793
mkvw1_10:
	s_waitcnt vmcnt(10)
	s_branch .LBB0_793
mkvw1_14:
	s_waitcnt vmcnt(14)
	s_branch .LBB0_793
mkvw1_16:
	s_waitcnt vmcnt(16)
	s_branch .LBB0_793
mkvw1_18:
	s_waitcnt vmcnt(18)
	s_branch .LBB0_793
mkvw1_20:
	s_waitcnt vmcnt(20)
	s_branch .LBB0_793
mkvw1_12:
	s_waitcnt vmcnt(12)
	s_branch .LBB0_793
mkvw1_22:
	s_waitcnt vmcnt(22)
	s_branch .LBB0_793
mkvw1_6:
	s_waitcnt vmcnt(6)

.LBB0_819:
	s_add_i32 s78, s87, 1
	s_min_u32 s78, s78, 3
	s_lshl_b32 s78, s78, 1
	s_cmp_gt_i32 s68, 63
	s_cselect_b64 s[84:85], -1, 0
	s_and_b64 s[80:81], s[84:85], exec
	s_cselect_b32 s80, 8, 16
	s_min_i32 s81, s87, 2
	s_lshl_b32 s81, s81, 1
	s_add_i32 s81, s81, 8
	s_cmp_lg_u32 s73, 63
	s_cselect_b32 s81, s81, 8
	s_and_b32 vcc_lo, s79, -2
	s_or_b32 s80, s78, s80
	s_cmp_eq_u32 s79, 4
	s_cselect_b32 s78, s81, s78
	s_cmp_eq_u32 vcc_lo, 2
	s_cselect_b32 s78, s80, s78
	s_cmp_eq_u32 s78, 6
	s_cbranch_scc1 mkvw2_6
	s_cmp_gt_u32 s78, 21
	s_cbranch_scc1 mkvw2_22
	s_cmp_eq_u32 s78, 12
	s_cbranch_scc1 mkvw2_12
	s_cmp_gt_u32 s78, 19
	s_cbranch_scc1 mkvw2_20
	s_cmp_gt_u32 s78, 17
	s_cbranch_scc1 mkvw2_18
	s_cmp_gt_u32 s78, 15
	s_cbranch_scc1 mkvw2_16
	s_cmp_gt_u32 s78, 13
	s_cbranch_scc1 mkvw2_14
	s_cmp_gt_u32 s78, 11
	s_cbranch_scc1 mkvw2_12
	s_cmp_gt_u32 s78, 9
	s_cbranch_scc1 mkvw2_10
	s_cmp_gt_u32 s78, 7
	s_cbranch_scc1 mkvw2_8
	s_cmp_gt_u32 s78, 5
	s_cbranch_scc1 mkvw2_6
	s_cmp_gt_u32 s78, 3
	s_cbranch_scc1 mkvw2_4
	s_cmp_gt_u32 s78, 1
	s_cbranch_scc1 mkvw2_2
mkvw2_0:
	s_waitcnt vmcnt(0)
	s_branch .LBB0_863
mkvw2_2:
	s_waitcnt vmcnt(2)
	s_branch .LBB0_863
mkvw2_4:
	s_waitcnt vmcnt(4)
	s_branch .LBB0_863
mkvw2_8:
	s_waitcnt vmcnt(8)
	s_branch .LBB0_863
mkvw2_10:
	s_waitcnt vmcnt(10)
	s_branch .LBB0_863
mkvw2_14:
	s_waitcnt vmcnt(14)
	s_branch .LBB0_863
mkvw2_16:
	s_waitcnt vmcnt(16)
	s_branch .LBB0_863
mkvw2_18:
	s_waitcnt vmcnt(18)
	s_branch .LBB0_863
mkvw2_20:
	s_waitcnt vmcnt(20)
	s_branch .LBB0_863
mkvw2_12:
	s_waitcnt vmcnt(12)
	s_branch .LBB0_863
mkvw2_22:
	s_waitcnt vmcnt(22)
	s_branch .LBB0_863
mkvw2_6:
	s_waitcnt vmcnt(6)
